# s5
# speedup vs baseline: 1.0076x; 1.0019x over previous
.LBB1_36:
	s_or_b64 exec, exec, s[10:11]
	v_fma_f32 v34, v21, v36, 0
	s_waitcnt lgkmcnt(1)
	v_fma_f32 v35, v21, v38, 0
	v_fmac_f32_e32 v34, v29, v28
	v_fmac_f32_e32 v35, v29, v39
	v_fmac_f32_e32 v34, v30, v32
	s_waitcnt lgkmcnt(0)
	v_fmac_f32_e32 v35, v30, v26
	v_fmac_f32_e32 v34, v33, v20
	v_fmac_f32_e32 v35, v33, v27
	s_waitcnt vmcnt(6)
	v_mov_b32_dpp v33, v120 row_newbcast:10 row_mask:0xf bank_mask:0xf bound_ctrl:1
	v_mov_b32_dpp v36, v120 row_newbcast:11 row_mask:0xf bank_mask:0xf bound_ctrl:1
	v_cmp_eq_u32_e64 s[10:11], 1, v57
	v_mov_b32_dpp v32, v120 row_newbcast:9 row_mask:0xf bank_mask:0xf bound_ctrl:1
	v_mov_b32_dpp v38, v120 row_newbcast:13 row_mask:0xf bank_mask:0xf bound_ctrl:1
	v_mov_b32_dpp v39, v120 row_newbcast:14 row_mask:0xf bank_mask:0xf bound_ctrl:1
	v_cndmask_b32_e64 v33, v36, v33, s[10:11]
	v_cmp_eq_u32_e64 s[8:9], 0, v57
	v_mov_b32_dpp v37, v120 row_newbcast:12 row_mask:0xf bank_mask:0xf bound_ctrl:1
	v_mov_b32_dpp v27, v120 row_newbcast:0 row_mask:0xf bank_mask:0xf bound_ctrl:1
	v_cndmask_b32_e64 v32, v33, v32, s[8:9]
	v_cndmask_b32_e64 v33, v39, v38, s[10:11]
	v_cndmask_b32_e64 v33, v33, v37, s[8:9]
	v_fma_f32 v33, v34, v33, -v35
	v_fma_f32 v32, v18, v33, -v32
	v_mov_b32_dpp v20, v120 row_newbcast:1 row_mask:0xf bank_mask:0xf bound_ctrl:1
	v_mov_b32_dpp v19, v120 row_newbcast:2 row_mask:0xf bank_mask:0xf bound_ctrl:1
	v_mov_b32_dpp v31, v120 row_newbcast:3 row_mask:0xf bank_mask:0xf bound_ctrl:1
	v_mov_b32_dpp v29, v120 row_newbcast:4 row_mask:0xf bank_mask:0xf bound_ctrl:1
	v_mov_b32_dpp v26, v120 row_newbcast:5 row_mask:0xf bank_mask:0xf bound_ctrl:1
	v_mov_b32_dpp v30, v120 row_newbcast:6 row_mask:0xf bank_mask:0xf bound_ctrl:1
	v_mov_b32_dpp v28, v120 row_newbcast:7 row_mask:0xf bank_mask:0xf bound_ctrl:1
	v_mov_b32_dpp v21, v120 row_newbcast:8 row_mask:0xf bank_mask:0xf bound_ctrl:1
	v_mov_b32_dpp v18, v32 quad_perm:[0,0,0,0] row_mask:0xf bank_mask:0xf bound_ctrl:1
	v_mov_b32_dpp v33, v32 quad_perm:[1,1,1,1] row_mask:0xf bank_mask:0xf bound_ctrl:1
	v_mov_b32_dpp v32, v32 quad_perm:[2,2,2,2] row_mask:0xf bank_mask:0xf bound_ctrl:1
	s_and_b64 s[12:13], vcc, s[4:5]
	s_and_b64 exec, exec, s[12:13]
	s_cbranch_execz .LBB1_39
	v_mul_f32_e32 v31, v31, v33
	v_fmac_f32_e32 v31, v27, v18
	v_mul_f32_e32 v27, v29, v33
	v_fmac_f32_e32 v27, v20, v18
	v_fmac_f32_e32 v27, v28, v32
	v_mul_f32_e32 v20, v26, v33
	v_fmac_f32_e32 v31, v30, v32
	v_fmac_f32_e32 v20, v19, v18
	v_mul_f32_e32 v18, v27, v27
	v_fmac_f32_e32 v20, v21, v32
	v_fmac_f32_e32 v18, v31, v31
	v_fmac_f32_e32 v18, v20, v20
	v_mad_u32_u24 v26, v56, 3, v57
	v_sqrt_f32_e32 v18, v18
	v_cndmask_b32_e64 v19, v20, v27, s[10:11]
	v_add_u32_e32 v29, 56, v26
	v_add_f32_e32 v21, 0x38d1b717, v18
	v_rcp_f32_e32 v21, v21
	v_cndmask_b32_e64 v20, v19, v31, s[8:9]
	v_mul_u32_u24_e32 v28, 0x2493, v26
	v_mul_u32_u24_e32 v30, 0x2493, v29
	v_lshrrev_b32_e32 v28, 16, v28
	v_lshrrev_b32_e32 v30, 16, v30
	v_mul_u32_u24_e32 v28, 66, v28
	v_mul_u32_u24_e32 v30, 66, v30
	v_lshl_add_u32 v28, v26, 1, v28
	v_lshl_add_u32 v30, v29, 1, v30
	v_cvt_f16_f32_e32 v27, v20
	v_fma_mixlo_f16 v20, v20, v21, 0
	ds_write_b16 v28, v27 offset:14368
	ds_write_b16 v30, v20 offset:14368
	s_and_b64 exec, exec, s[8:9]
	s_cbranch_execz .LBB1_39
	v_cmp_lt_u32_e32 vcc, 6, v56
	v_cvt_f16_f32_e32 v18, v18
	v_lshlrev_b32_e32 v19, 1, v56
	v_mov_b32_e32 v20, 0x42
	v_cndmask_b32_e32 v20, 0, v20, vcc
	v_add_u32_e32 v19, v19, v20
	ds_write_b16 v19, v18 offset:14848
